# baseline (speedup 1.0000x reference)
.LBB0_8:
	s_load_dwordx4 s[4:7], s[0:1], 0x0
	v_and_b32_e32 v1, 63, v0
	s_cmpk_gt_i32 s12, 0xff
	s_mov_b64 s[2:3], -1
	s_cbranch_scc0 .LBB0_24
	v_and_b32_e32 v74, 31, v0
	v_lshrrev_b32_e32 v75, 5, v1
	v_lshrrev_b32_e32 v76, 6, v0
	s_lshl_b32 s8, s12, 2
	s_cmpk_gt_u32 s12, 0x1ff
	v_mov_b32_e32 v39, 0
	v_add_u32_e32 v77, s8, v76
	v_lshlrev_b32_e32 v36, 2, v74
	v_lshlrev_b32_e32 v34, 17, v75
	s_cbranch_scc0 .LBB0_11
	v_add_u32_e32 v4, 0xfffff800, v77
	s_load_dwordx2 s[2:3], s[0:1], 0x30
	v_lshrrev_b32_e32 v2, 2, v4
	v_and_b32_e32 v38, 0x3fffffc0, v2
	v_lshlrev_b64 v[2:3], 14, v[38:39]
	v_lshlrev_b32_e32 v4, 6, v4
	v_bfe_u32 v78, v0, 6, 1
	s_waitcnt lgkmcnt(0)
	v_lshl_add_u64 v[2:3], s[6:7], 0, v[2:3]
	v_and_b32_e32 v40, 0x3f80, v4
	v_mov_b32_e32 v41, v39
	v_lshlrev_b32_e32 v4, 8, v74
	v_lshl_add_u64 v[2:3], v[2:3], 0, v[40:41]
	v_mov_b32_e32 v37, v39
	v_lshl_or_b32 v4, v78, 13, v4
	v_mov_b32_e32 v5, v39
	v_lshl_add_u64 v[2:3], v[2:3], 0, v[36:37]
	v_lshl_add_u64 v[4:5], s[2:3], 0, v[4:5]
	v_lshlrev_b32_e32 v6, 5, v75
	v_mov_b32_e32 v7, v39
	v_mov_b32_e32 v35, v39
	v_lshl_add_u64 v[42:43], v[4:5], 0, v[6:7]
	v_lshl_add_u64 v[44:45], v[2:3], 0, v[34:35]
	s_movk_i32 s2, 0x4000
	global_load_dwordx4 v[26:29], v[42:43], off offset:16
	global_load_dwordx4 v[30:33], v[42:43], off
	global_load_dwordx4 v[18:21], v[42:43], off offset:80
	global_load_dwordx4 v[22:25], v[42:43], off offset:64
	global_load_dwordx4 v[10:13], v[42:43], off offset:144
	global_load_dwordx4 v[14:17], v[42:43], off offset:128
	global_load_dwordx4 v[2:5], v[42:43], off offset:208
	global_load_dwordx4 v[6:9], v[42:43], off offset:192
	v_add_co_u32_e32 v42, vcc, s2, v44
	s_mov_b32 s3, 0x8000
	s_nop 0
	v_addc_co_u32_e32 v43, vcc, 0, v45, vcc
	v_add_co_u32_e32 v46, vcc, s3, v44
	s_mov_b32 s8, 0xc000
	s_nop 0
	v_addc_co_u32_e32 v47, vcc, 0, v45, vcc
	v_add_co_u32_e32 v48, vcc, s8, v44
	s_mov_b32 s9, 0x10000
	s_nop 0
	v_addc_co_u32_e32 v49, vcc, 0, v45, vcc
	v_add_co_u32_e32 v50, vcc, s9, v44
	s_mov_b32 s9, 0x14000
	s_nop 0
	v_addc_co_u32_e32 v51, vcc, 0, v45, vcc
	v_add_co_u32_e32 v52, vcc, s9, v44
	s_mov_b32 s9, 0x18000
	s_nop 0
	v_addc_co_u32_e32 v53, vcc, 0, v45, vcc
	v_add_co_u32_e32 v54, vcc, s9, v44
	s_mov_b32 s9, 0x1c000
	s_nop 0
	v_addc_co_u32_e32 v55, vcc, 0, v45, vcc
	v_add_co_u32_e32 v56, vcc, s9, v44
	s_mov_b32 s9, 0x40000
	s_nop 0
	v_addc_co_u32_e32 v57, vcc, 0, v45, vcc
	global_load_dword v72, v[44:45], off
	global_load_dword v73, v[42:43], off
	global_load_dword v70, v[46:47], off
	global_load_dword v71, v[48:49], off
	global_load_dword v68, v[50:51], off
	global_load_dword v69, v[52:53], off
	global_load_dword v66, v[54:55], off
	global_load_dword v67, v[56:57], off
	v_add_co_u32_e32 v42, vcc, s9, v44
	s_mov_b32 s10, 0x44000
	s_nop 0
	v_addc_co_u32_e32 v43, vcc, 0, v45, vcc
	v_add_co_u32_e32 v46, vcc, s10, v44
	s_mov_b32 s11, 0x48000
	s_nop 0
	v_addc_co_u32_e32 v47, vcc, 0, v45, vcc
	v_add_co_u32_e32 v48, vcc, s11, v44
	s_mov_b32 s13, 0x4c000
	s_nop 0
	v_addc_co_u32_e32 v49, vcc, 0, v45, vcc
	v_add_co_u32_e32 v50, vcc, s13, v44
	s_mov_b32 s14, 0x50000
	s_nop 0
	v_addc_co_u32_e32 v51, vcc, 0, v45, vcc
	v_add_co_u32_e32 v52, vcc, s14, v44
	s_mov_b32 s14, 0x54000
	s_nop 0
	v_addc_co_u32_e32 v53, vcc, 0, v45, vcc
	v_add_co_u32_e32 v54, vcc, s14, v44
	s_mov_b32 s14, 0x58000
	s_nop 0
	v_addc_co_u32_e32 v55, vcc, 0, v45, vcc
	v_add_co_u32_e32 v56, vcc, s14, v44
	s_mov_b32 s14, 0x5c000
	s_nop 0
	v_addc_co_u32_e32 v57, vcc, 0, v45, vcc
	v_add_co_u32_e32 v80, vcc, s14, v44
	s_mov_b32 s14, 0x80000
	s_nop 0
	v_addc_co_u32_e32 v81, vcc, 0, v45, vcc
	global_load_dword v64, v[42:43], off
	global_load_dword v65, v[46:47], off
	global_load_dword v62, v[48:49], off
	global_load_dword v63, v[50:51], off
	global_load_dword v60, v[52:53], off
	global_load_dword v61, v[54:55], off
	global_load_dword v58, v[56:57], off
	global_load_dword v59, v[80:81], off
	v_add_co_u32_e32 v42, vcc, s14, v44
	s_mov_b32 s14, 0x84000
	s_nop 0
	v_addc_co_u32_e32 v43, vcc, 0, v45, vcc
	v_add_co_u32_e32 v46, vcc, s14, v44
	s_mov_b32 s14, 0x88000
	s_nop 0
	v_addc_co_u32_e32 v47, vcc, 0, v45, vcc
	v_add_co_u32_e32 v48, vcc, s14, v44
	s_mov_b32 s14, 0x8c000
	s_nop 0
	v_addc_co_u32_e32 v49, vcc, 0, v45, vcc
	v_add_co_u32_e32 v54, vcc, s14, v44
	s_mov_b32 s14, 0x90000
	s_nop 0
	v_addc_co_u32_e32 v55, vcc, 0, v45, vcc
	v_add_co_u32_e32 v80, vcc, s14, v44
	s_mov_b32 s14, 0x94000
	s_nop 0
	v_addc_co_u32_e32 v81, vcc, 0, v45, vcc
	v_add_co_u32_e32 v82, vcc, s14, v44
	s_mov_b32 s14, 0x98000
	s_nop 0
	v_addc_co_u32_e32 v83, vcc, 0, v45, vcc
	global_load_dword v56, v[42:43], off
	global_load_dword v57, v[46:47], off
	global_load_dword v52, v[48:49], off
	global_load_dword v53, v[54:55], off
	global_load_dword v50, v[80:81], off
	global_load_dword v51, v[82:83], off
	v_add_co_u32_e32 v42, vcc, s14, v44
	s_mov_b32 s14, 0x9c000
	s_nop 0
	v_addc_co_u32_e32 v43, vcc, 0, v45, vcc
	v_add_co_u32_e32 v46, vcc, s14, v44
	s_mov_b32 s14, 0xc0000
	s_nop 0
	v_addc_co_u32_e32 v47, vcc, 0, v45, vcc
	global_load_dword v54, v[42:43], off
	global_load_dword v55, v[46:47], off
	v_add_co_u32_e32 v80, vcc, s14, v44
	s_mov_b32 s14, 0xc4000
	s_nop 0
	v_addc_co_u32_e32 v81, vcc, 0, v45, vcc
	v_add_co_u32_e32 v82, vcc, s14, v44
	s_mov_b32 s14, 0xc8000
	s_nop 0
	v_addc_co_u32_e32 v83, vcc, 0, v45, vcc
	v_add_co_u32_e32 v84, vcc, s14, v44
	s_mov_b32 s14, 0xcc000
	s_nop 0
	v_addc_co_u32_e32 v85, vcc, 0, v45, vcc
	v_add_co_u32_e32 v86, vcc, s14, v44
	s_mov_b32 s14, 0xd0000
	s_nop 0
	v_addc_co_u32_e32 v87, vcc, 0, v45, vcc
	v_add_co_u32_e32 v88, vcc, s14, v44
	s_mov_b32 s14, 0xd4000
	s_nop 0
	v_addc_co_u32_e32 v89, vcc, 0, v45, vcc
	v_add_co_u32_e32 v90, vcc, s14, v44
	s_mov_b32 s14, 0xd8000
	s_nop 0
	v_addc_co_u32_e32 v91, vcc, 0, v45, vcc
	v_add_co_u32_e32 v92, vcc, s14, v44
	s_mov_b32 s14, 0xdc000
	s_nop 0
	v_addc_co_u32_e32 v93, vcc, 0, v45, vcc
	v_add_co_u32_e32 v94, vcc, s14, v44
	s_load_dwordx2 s[14:15], s[0:1], 0x58
	s_nop 0
	v_addc_co_u32_e32 v95, vcc, 0, v45, vcc
	global_load_dword v48, v[80:81], off
	global_load_dword v49, v[82:83], off
	global_load_dword v46, v[84:85], off
	global_load_dword v47, v[86:87], off
	global_load_dword v44, v[88:89], off
	global_load_dword v45, v[90:91], off
	global_load_dword v42, v[92:93], off
	global_load_dword v43, v[94:95], off
	s_waitcnt vmcnt(38)
	s_waitcnt vmcnt(31)
	s_waitcnt vmcnt(30)
	s_waitcnt vmcnt(29)
	s_waitcnt vmcnt(28)
	s_waitcnt vmcnt(27)
	s_waitcnt vmcnt(26)
	s_waitcnt vmcnt(25)
	s_waitcnt vmcnt(24)
	s_waitcnt vmcnt(23)
	s_waitcnt vmcnt(22)
	s_waitcnt vmcnt(21)
	s_waitcnt vmcnt(20)
	s_waitcnt vmcnt(19)
	s_waitcnt vmcnt(18)
	s_waitcnt vmcnt(17)
	s_waitcnt vmcnt(16)
	v_cvt_pk_bf16_f32 v35, v72, 0
	v_cvt_pk_bf16_f32 v79, v73, 0
	v_lshlrev_b32_e32 v81, 16, v79
	v_lshlrev_b32_e32 v80, 16, v35
	v_pk_add_f32 v[82:83], v[72:73], v[80:81] neg_lo:[0,1] neg_hi:[0,1]
	v_cvt_pk_bf16_f32 v35, v70, 0
	v_cvt_pk_bf16_f32 v73, v71, 0
	v_lshlrev_b32_e32 v72, 16, v35
	v_lshlrev_b32_e32 v73, 16, v73
	v_pk_add_f32 v[84:85], v[70:71], v[72:73] neg_lo:[0,1] neg_hi:[0,1]
	v_cvt_pk_bf16_f32 v35, v68, 0
	v_cvt_pk_bf16_f32 v70, v69, 0
	v_lshlrev_b32_e32 v86, 16, v35
	v_lshlrev_b32_e32 v87, 16, v70
	v_pk_add_f32 v[88:89], v[68:69], v[86:87] neg_lo:[0,1] neg_hi:[0,1]
	v_cvt_pk_bf16_f32 v35, v66, 0
	v_cvt_pk_bf16_f32 v68, v67, 0
	v_lshlrev_b32_e32 v90, 16, v35
	v_lshlrev_b32_e32 v91, 16, v68
	v_pk_add_f32 v[92:93], v[66:67], v[90:91] neg_lo:[0,1] neg_hi:[0,1]
	v_cvt_pk_bf16_f32 v35, v30, 0
	v_cvt_pk_bf16_f32 v66, v31, 0
	v_cvt_pk_bf16_f32 v68, v26, 0
	v_lshlrev_b32_e32 v67, 16, v66
	v_lshlrev_b32_e32 v66, 16, v35
	v_cvt_pk_bf16_f32 v35, v27, 0
	v_lshlrev_b32_e32 v69, 16, v35
	v_lshlrev_b32_e32 v68, 16, v68
	v_pk_add_f32 v[94:95], v[26:27], v[68:69] neg_lo:[0,1] neg_hi:[0,1]
	v_cvt_pk_bf16_f32 v26, v32, 0
	v_cvt_pk_bf16_f32 v35, v28, 0
	v_cvt_pk_bf16_f32 v27, v33, 0
	v_cvt_pk_bf16_f32 v70, v29, 0
	v_lshlrev_b32_e32 v26, 16, v26
	v_lshlrev_b32_e32 v27, 16, v27
	v_lshlrev_b32_e32 v96, 16, v35
	v_lshlrev_b32_e32 v97, 16, v70
	v_pk_add_f32 v[30:31], v[30:31], v[66:67] neg_lo:[0,1] neg_hi:[0,1]
	v_cvt_pk_bf16_f32 v66, v66, v67
	v_cvt_pk_bf16_f32 v67, v26, v27
	v_cvt_pk_bf16_f32 v68, v68, v69
	v_cvt_pk_bf16_f32 v69, v96, v97
	v_cvt_pk_bf16_f32 v70, v80, v81
	v_cvt_pk_bf16_f32 v71, v72, v73
	v_cvt_pk_bf16_f32 v72, v86, v87
	v_cvt_pk_bf16_f32 v73, v90, v91
	v_pk_add_f32 v[32:33], v[32:33], v[26:27] neg_lo:[0,1] neg_hi:[0,1]
	v_pk_add_f32 v[80:81], v[28:29], v[96:97] neg_lo:[0,1] neg_hi:[0,1]
	v_mfma_f32_32x32x16_bf16 a[0:15], v[66:69], v[70:73], 0
	v_cvt_pk_bf16_f32 v26, v82, v83
	v_cvt_pk_bf16_f32 v27, v84, v85
	v_cvt_pk_bf16_f32 v28, v88, v89
	v_cvt_pk_bf16_f32 v29, v92, v93
	v_cvt_pk_bf16_f32 v30, v30, v31
	v_cvt_pk_bf16_f32 v31, v32, v33
	v_cvt_pk_bf16_f32 v32, v94, v95
	v_mfma_f32_32x32x16_bf16 a[0:15], v[66:69], v[26:29], a[0:15]
	v_cvt_pk_bf16_f32 v33, v80, v81
	v_cvt_pk_bf16_f32 v26, v64, 0
	v_cvt_pk_bf16_f32 v27, v65, 0
	v_cvt_pk_bf16_f32 v28, v18, 0
	v_cvt_pk_bf16_f32 v29, v19, 0
	v_lshlrev_b32_e32 v29, 16, v29
	v_lshlrev_b32_e32 v28, 16, v28
	v_mfma_f32_32x32x16_bf16 a[0:15], v[30:33], v[70:73], a[0:15]
	v_lshlrev_b32_e32 v30, 16, v26
	v_lshlrev_b32_e32 v31, 16, v27
	v_cvt_pk_bf16_f32 v26, v62, 0
	v_cvt_pk_bf16_f32 v27, v63, 0
	v_lshlrev_b32_e32 v32, 16, v26
	v_lshlrev_b32_e32 v33, 16, v27
	v_cvt_pk_bf16_f32 v26, v60, 0
	v_cvt_pk_bf16_f32 v27, v61, 0
	v_lshlrev_b32_e32 v66, 16, v26
	v_lshlrev_b32_e32 v67, 16, v27
	v_cvt_pk_bf16_f32 v26, v58, 0
	v_cvt_pk_bf16_f32 v27, v59, 0
	v_lshlrev_b32_e32 v68, 16, v26
	v_lshlrev_b32_e32 v69, 16, v27
	v_cvt_pk_bf16_f32 v26, v22, 0
	v_cvt_pk_bf16_f32 v27, v23, 0
	v_pk_add_f32 v[70:71], v[18:19], v[28:29] neg_lo:[0,1] neg_hi:[0,1]
	v_cvt_pk_bf16_f32 v18, v24, 0
	v_cvt_pk_bf16_f32 v35, v20, 0
	v_cvt_pk_bf16_f32 v19, v25, 0
	v_cvt_pk_bf16_f32 v73, v21, 0
	v_lshlrev_b32_e32 v27, 16, v27
	v_lshlrev_b32_e32 v26, 16, v26
	v_lshlrev_b32_e32 v18, 16, v18
	v_lshlrev_b32_e32 v19, 16, v19
	v_lshlrev_b32_e32 v72, 16, v35
	v_lshlrev_b32_e32 v73, 16, v73
	v_pk_add_f32 v[22:23], v[22:23], v[26:27] neg_lo:[0,1] neg_hi:[0,1]
	v_cvt_pk_bf16_f32 v26, v26, v27
	v_cvt_pk_bf16_f32 v27, v18, v19
	v_cvt_pk_bf16_f32 v28, v28, v29
	v_cvt_pk_bf16_f32 v29, v72, v73
	v_pk_add_f32 v[64:65], v[64:65], v[30:31] neg_lo:[0,1] neg_hi:[0,1]
	v_pk_add_f32 v[62:63], v[62:63], v[32:33] neg_lo:[0,1] neg_hi:[0,1]
	v_cvt_pk_bf16_f32 v30, v30, v31
	v_cvt_pk_bf16_f32 v31, v32, v33
	v_cvt_pk_bf16_f32 v32, v66, v67
	v_cvt_pk_bf16_f32 v33, v68, v69
	v_pk_add_f32 v[60:61], v[60:61], v[66:67] neg_lo:[0,1] neg_hi:[0,1]
	v_pk_add_f32 v[58:59], v[58:59], v[68:69] neg_lo:[0,1] neg_hi:[0,1]
	v_mfma_f32_32x32x16_bf16 a[0:15], v[26:29], v[30:33], a[0:15]
	v_add_f32_e64 v24, v24, -v18
	v_add_f32_e64 v25, v25, -v19
	v_add_f32_e64 v66, v20, -v72
	v_add_f32_e64 v67, v21, -v73
	v_cvt_pk_bf16_f32 v18, v64, v65
	v_cvt_pk_bf16_f32 v19, v62, v63
	v_cvt_pk_bf16_f32 v20, v60, v61
	v_cvt_pk_bf16_f32 v21, v58, v59
	v_cvt_pk_bf16_f32 v22, v22, v23
	v_cvt_pk_bf16_f32 v23, v24, v25
	v_mfma_f32_32x32x16_bf16 a[0:15], v[26:29], v[18:21], a[0:15]
	v_cvt_pk_bf16_f32 v24, v70, v71
	v_cvt_pk_bf16_f32 v25, v66, v67
	s_waitcnt vmcnt(15)
	s_waitcnt vmcnt(14)
	s_waitcnt vmcnt(13)
	s_waitcnt vmcnt(12)
	s_waitcnt vmcnt(11)
	s_waitcnt vmcnt(10)
	s_waitcnt vmcnt(9)
	s_waitcnt vmcnt(8)
	v_cvt_pk_bf16_f32 v20, v10, 0
	v_cvt_pk_bf16_f32 v18, v56, 0
	v_cvt_pk_bf16_f32 v19, v57, 0
	v_mfma_f32_32x32x16_bf16 a[0:15], v[22:25], v[30:33], a[0:15]
	v_lshlrev_b32_e32 v22, 16, v18
	v_lshlrev_b32_e32 v23, 16, v19
	v_cvt_pk_bf16_f32 v18, v52, 0
	v_cvt_pk_bf16_f32 v19, v53, 0
	v_lshlrev_b32_e32 v24, 16, v18
	v_lshlrev_b32_e32 v25, 16, v19
	v_cvt_pk_bf16_f32 v18, v50, 0
	v_cvt_pk_bf16_f32 v19, v51, 0
	v_lshlrev_b32_e32 v30, 16, v18
	v_lshlrev_b32_e32 v31, 16, v19
	v_cvt_pk_bf16_f32 v18, v54, 0
	v_cvt_pk_bf16_f32 v19, v55, 0
	v_cvt_pk_bf16_f32 v21, v11, 0
	v_pk_add_f32 v[32:33], v[50:51], v[30:31] neg_lo:[0,1] neg_hi:[0,1]
	v_lshlrev_b32_e32 v50, 16, v18
	v_lshlrev_b32_e32 v51, 16, v19
	v_lshlrev_b32_e32 v21, 16, v21
	v_lshlrev_b32_e32 v20, 16, v20
	v_pk_add_f32 v[26:27], v[56:57], v[22:23] neg_lo:[0,1] neg_hi:[0,1]
	v_pk_add_f32 v[28:29], v[52:53], v[24:25] neg_lo:[0,1] neg_hi:[0,1]
	v_pk_add_f32 v[52:53], v[54:55], v[50:51] neg_lo:[0,1] neg_hi:[0,1]
	v_cvt_pk_bf16_f32 v18, v14, 0
	v_cvt_pk_bf16_f32 v19, v15, 0
	v_pk_add_f32 v[54:55], v[10:11], v[20:21] neg_lo:[0,1] neg_hi:[0,1]
	v_cvt_pk_bf16_f32 v10, v16, 0
	v_cvt_pk_bf16_f32 v35, v12, 0
	v_cvt_pk_bf16_f32 v11, v17, 0
	v_cvt_pk_bf16_f32 v57, v13, 0
	v_lshlrev_b32_e32 v19, 16, v19
	v_lshlrev_b32_e32 v18, 16, v18
	v_lshlrev_b32_e32 v10, 16, v10
	v_lshlrev_b32_e32 v11, 16, v11
	v_lshlrev_b32_e32 v56, 16, v35
	v_lshlrev_b32_e32 v57, 16, v57
	v_pk_add_f32 v[14:15], v[14:15], v[18:19] neg_lo:[0,1] neg_hi:[0,1]
	v_cvt_pk_bf16_f32 v18, v18, v19
	v_cvt_pk_bf16_f32 v19, v10, v11
	v_cvt_pk_bf16_f32 v20, v20, v21
	v_cvt_pk_bf16_f32 v21, v56, v57
	v_cvt_pk_bf16_f32 v22, v22, v23
	v_cvt_pk_bf16_f32 v23, v24, v25
	v_cvt_pk_bf16_f32 v24, v30, v31
	v_cvt_pk_bf16_f32 v25, v50, v51
	v_pk_add_f32 v[16:17], v[16:17], v[10:11] neg_lo:[0,1] neg_hi:[0,1]
	v_pk_add_f32 v[30:31], v[12:13], v[56:57] neg_lo:[0,1] neg_hi:[0,1]
	v_mfma_f32_32x32x16_bf16 a[0:15], v[18:21], v[22:25], a[0:15]
	v_cvt_pk_bf16_f32 v10, v26, v27
	v_cvt_pk_bf16_f32 v11, v28, v29
	v_cvt_pk_bf16_f32 v12, v32, v33
	v_cvt_pk_bf16_f32 v13, v52, v53
	v_cvt_pk_bf16_f32 v14, v14, v15
	v_cvt_pk_bf16_f32 v15, v16, v17
	v_cvt_pk_bf16_f32 v16, v54, v55
	v_mfma_f32_32x32x16_bf16 a[0:15], v[18:21], v[10:13], a[0:15]
	v_cvt_pk_bf16_f32 v17, v30, v31
	s_waitcnt vmcnt(7)
	s_waitcnt vmcnt(6)
	s_waitcnt vmcnt(5)
	s_waitcnt vmcnt(4)
	s_waitcnt vmcnt(3)
	s_waitcnt vmcnt(2)
	s_waitcnt vmcnt(1)
	s_waitcnt vmcnt(0)
	v_lshl_or_b32 v38, v78, 5, v38
	v_cvt_pk_bf16_f32 v10, v48, 0
	v_cvt_pk_bf16_f32 v11, v49, 0
	v_mfma_f32_32x32x16_bf16 a[0:15], v[14:17], v[22:25], a[0:15]
	v_lshlrev_b32_e32 v14, 16, v10
	v_lshlrev_b32_e32 v15, 16, v11
	v_cvt_pk_bf16_f32 v10, v46, 0
	v_cvt_pk_bf16_f32 v11, v47, 0
	v_lshlrev_b32_e32 v16, 16, v10
	v_lshlrev_b32_e32 v17, 16, v11
	v_cvt_pk_bf16_f32 v10, v44, 0
	v_cvt_pk_bf16_f32 v11, v45, 0
	v_cvt_pk_bf16_f32 v12, v2, 0
	v_cvt_pk_bf16_f32 v13, v3, 0
	v_lshlrev_b32_e32 v22, 16, v10
	v_lshlrev_b32_e32 v23, 16, v11
	v_cvt_pk_bf16_f32 v10, v42, 0
	v_cvt_pk_bf16_f32 v11, v43, 0
	v_lshlrev_b32_e32 v13, 16, v13
	v_lshlrev_b32_e32 v12, 16, v12
	v_lshlrev_b32_e32 v26, 16, v10
	v_lshlrev_b32_e32 v27, 16, v11
	v_cvt_pk_bf16_f32 v10, v6, 0
	v_cvt_pk_bf16_f32 v11, v7, 0
	v_pk_add_f32 v[30:31], v[2:3], v[12:13] neg_lo:[0,1] neg_hi:[0,1]
	v_cvt_pk_bf16_f32 v2, v8, 0
	v_cvt_pk_bf16_f32 v32, v4, 0
	v_cvt_pk_bf16_f32 v3, v9, 0
	v_cvt_pk_bf16_f32 v33, v5, 0
	v_lshlrev_b32_e32 v11, 16, v11
	v_lshlrev_b32_e32 v10, 16, v10
	v_lshlrev_b32_e32 v2, 16, v2
	v_lshlrev_b32_e32 v3, 16, v3
	v_lshlrev_b32_e32 v32, 16, v32
	v_lshlrev_b32_e32 v33, 16, v33
	v_pk_add_f32 v[6:7], v[6:7], v[10:11] neg_lo:[0,1] neg_hi:[0,1]
	v_cvt_pk_bf16_f32 v10, v10, v11
	v_cvt_pk_bf16_f32 v11, v2, v3
	v_cvt_pk_bf16_f32 v12, v12, v13
	v_cvt_pk_bf16_f32 v13, v32, v33
	v_pk_add_f32 v[18:19], v[48:49], v[14:15] neg_lo:[0,1] neg_hi:[0,1]
	v_pk_add_f32 v[20:21], v[46:47], v[16:17] neg_lo:[0,1] neg_hi:[0,1]
	v_cvt_pk_bf16_f32 v14, v14, v15
	v_cvt_pk_bf16_f32 v15, v16, v17
	v_cvt_pk_bf16_f32 v16, v22, v23
	v_cvt_pk_bf16_f32 v17, v26, v27
	v_pk_add_f32 v[24:25], v[44:45], v[22:23] neg_lo:[0,1] neg_hi:[0,1]
	v_pk_add_f32 v[28:29], v[42:43], v[26:27] neg_lo:[0,1] neg_hi:[0,1]
	v_mfma_f32_32x32x16_bf16 a[0:15], v[10:13], v[14:17], a[0:15]
	v_add_f32_e64 v8, v8, -v2
	v_add_f32_e64 v9, v9, -v3
	v_add_f32_e64 v22, v4, -v32
	v_add_f32_e64 v23, v5, -v33
	v_cvt_pk_bf16_f32 v2, v18, v19
	v_cvt_pk_bf16_f32 v3, v20, v21
	v_cvt_pk_bf16_f32 v4, v24, v25
	v_cvt_pk_bf16_f32 v5, v28, v29
	v_cvt_pk_bf16_f32 v6, v6, v7
	v_cvt_pk_bf16_f32 v7, v8, v9
	v_mfma_f32_32x32x16_bf16 a[0:15], v[10:13], v[2:5], a[0:15]
	v_cvt_pk_bf16_f32 v8, v30, v31
	v_cvt_pk_bf16_f32 v9, v22, v23
	v_lshrrev_b32_e32 v38, 6, v0
	s_lshl_b32 s2, s12, 2
	s_add_i32 s2, s2, 0xfffff800
	v_add_u32_e32 v38, s2, v38
	v_lshlrev_b32_e32 v38, 12, v38
	v_lshl_add_u32 v38, v1, 4, v38
	s_waitcnt lgkmcnt(0)
	v_mfma_f32_32x32x16_bf16 a[0:15], v[6:9], v[14:17], a[0:15]
	s_mov_b64 s[2:3], 0
	s_nop 7
	s_nop 4
	global_store_dwordx4 v38, a[0:3], s[14:15]
	global_store_dwordx4 v38, a[4:7], s[14:15] offset:1024
	global_store_dwordx4 v38, a[8:11], s[14:15] offset:2048
	global_store_dwordx4 v38, a[12:15], s[14:15] offset:3072
